# conversion slots rotated per XCD plus cache-touch of the SWA units K/V tiles at the start of the last diff unit, on top of nt loads + reversed P6
# baseline (speedup 1.0000x reference)
; template <bool HAVE_PREV, bool HAVE_NEXT> __device__ __forceinline__ void dstep(f32x16& ca, f32x16& cb, f32x16& pa, f32x16& pb, const bf16x8 (&kf)[4], bf16x8 (&kn)[4], const LAS unsigned char* kbn, unsigned vpa, ...
;     ...
;     ca = __builtin_amdgcn_mfma_f32_32x32x16_bf16(kf[0], qr[0], z, 0, 0, 0);
;     float a0, a1, a2, a3, a4, a5, a6, a7, b0, b1, b2, b3, b4, b5, b6, b7;
;     if (HAVE_PREV) { a0 = fadd_s(pa[0], pa[1]); a1 = fadd_s(pa[2], pa[3]); a2 = fadd_s(pa[4], pa[5]); a3 = fadd_s(pa[6], pa[7]); a4 = fadd_s(pa[8], pa[9]); a5 = fadd_s(pa[10], pa[11]); a6 = fadd_s(pa[12], pa[13]); a7 = fadd_s(pa[14], pa[15]);
;         wa[0].x = cvtpk(pa[0], pa[1]); wa[0].y = cvtpk(pa[2], pa[3]); wa[0].z = cvtpk(pa[4], pa[5]); wa[0].w = cvtpk(pa[6], pa[7]); }
;     ATT_SB();
;     ca = __builtin_amdgcn_mfma_f32_32x32x16_bf16(kf[1], qr[1], ca, 0, 0, 0);
;     if (HAVE_PREV) {
;         ATT_TR(vl[0][0], vpa, 0); ATT_TR(vh[0][0], vpa, 512); ATT_TR(vl[1][0], vpa, 4096); ATT_TR(vh[1][0], vpa, 4096 + 512);
;         ATT_TR(vl[0][1], vpa, 1024); ATT_TR(vh[0][1], vpa, 1024 + 512); ATT_TR(vl[1][1], vpa, 4096 + 1024); ATT_TR(vh[1][1], vpa, 4096 + 1024 + 512);
;         a0 = fadd_s(a0, a1); a2 = fadd_s(a2, a3); a4 = fadd_s(a4, a5); a6 = fadd_s(a6, a7);
;         wa[1].x = cvtpk(pa[8], pa[9]); wa[1].y = cvtpk(pa[10], pa[11]); wa[1].z = cvtpk(pa[12], pa[13]); wa[1].w = cvtpk(pa[14], pa[15]);
; __device__ __forceinline__ void unit_diff(const P& p, LAS unsigned char* lds, const Src& S, float lam, bf16_t* orow, const int wid,
;                                           bf16x8 (&qr)[4], const bool pre  , const bool pn  , const Src& Sn) {
;     ...
;     const int koff = hi * 1024 + r32 * 16;
;     const int voff = 8192 + ((lane >> 4) & 1) * 32 + (lane & 3) * 8 + (4 * hi + ((lane & 15) >> 2)) * 64;
;     const unsigned lbase = (unsigned)(__SIZE_TYPE__)lds;
;     f32x16 A0, B0, A1, B1; bf16x8 kA[4], kB[4];
;     ATT_WAITV(0); ATT_BAR(); ATT_DMA(2, 2 * SLOTB); ATT_DMA(3, 3 * SLOTB);
; #pragma unroll
;     for (int d0 = 0; d0 < 4; ++d0) kA[d0] = *(const LAS bf16x8*)(lds + koff + d0 * 2048);
;     dstep<false, true>(A0, B0, A1, B1, kA, kB, lds + koff + 512, 0u, qr, o1, o2, l1, l2);
;     dstep<true, true>(A1, B1, A0, B0, kB, kA, lds + SLOTB + koff, lbase + voff, qr, o1, o2, l1, l2);
;     int sl_prev = 0, sl_cur = SLOTB, sl_nxt = 2 * SLOTB, sl_n2 = 3 * SLOTB, sl_dma = 4 * SLOTB;
.LBB7_437:
	s_and_b32 s2, s58, 7
	s_lshl_b32 s10, s2, 13
	s_add_u32 s13, s79, s10
	s_addc_u32 s36, s80, 0
	s_add_u32 s10, s13, 0x8000
	s_addc_u32 s11, s36, 0
	v_lshlrev_b64 v[160:161], 1, v[0:1]
	s_add_u32 s13, s13, 0x18000
	s_waitcnt vmcnt(0)
	v_lshl_add_u64 v[0:1], s[56:57], 0, v[160:161]
	s_addc_u32 s36, s36, 0
	s_waitcnt lgkmcnt(0)
	s_barrier
	v_lshl_add_u64 v[2:3], v[0:1], 0, s[48:49]
	s_add_i32 m0, s96, 0x8000
	v_lshl_add_u64 v[0:1], v[0:1], 0, s[50:51]
	global_load_lds_dwordx4 v[2:3], off
	v_lshl_add_u64 v[2:3], s[54:55], 0, v[160:161]
	s_waitcnt vmcnt(0)
	v_lshl_add_u64 v[4:5], v[2:3], 0, s[48:49]
	s_mov_b32 m0, s42
	v_lshlrev_b32_e32 v49, 8, v170
	global_load_lds_dwordx4 v[4:5], off
	s_add_i32 m0, s96, 0xc000
	v_lshlrev_b32_e32 v4, 4, v169
	global_load_lds_dwordx4 v[0:1], off
	v_lshl_add_u64 v[0:1], v[2:3], 0, s[50:51]
	s_mov_b32 m0, s43
	v_lshlrev_b32_e32 v2, 3, v169
	global_load_lds_dwordx4 v[0:1], off
	v_lshlrev_b32_e32 v0, 4, v171
	v_lshl_or_b32 v0, v170, 10, v0
	v_lshlrev_b32_e32 v1, 1, v169
	v_and_b32_e32 v1, 32, v1
	v_add_u32_e32 v173, 0, v0
	v_and_or_b32 v48, v2, 24, v1
	ds_read_b128 v[0:3], v173
	s_waitcnt lgkmcnt(0)
	v_mfma_f32_32x32x16_bf16 v[16:31], v[0:3], v[128:131], 0
	v_and_b32_e32 v50, 0xc0, v4
	ds_read_b128 v[4:7], v173 offset:2048
	ds_read_b128 v[8:11], v173 offset:4096
	ds_read_b128 v[32:35], v173 offset:6144
	s_mov_b32 s59, 0x8000
	s_mov_b32 s37, 0xc000
	s_waitcnt lgkmcnt(0)
	v_mfma_f32_32x32x16_bf16 v[16:31], v[4:7], v[132:135], v[16:31]
	v_mfma_f32_32x32x16_bf16 v[0:15], v[8:11], v[136:139], 0
	v_mfma_f32_32x32x16_bf16 v[0:15], v[32:35], v[140:143], v[0:15]
	s_waitcnt lgkmcnt(0)
	ds_read_b128 v[36:39], v173 offset:512
	ds_read_b128 v[40:43], v173 offset:2560
	ds_read_b128 v[44:47], v173 offset:4608
	ds_read_b128 v[32:35], v173 offset:6656
	s_nop 5
	v_exp_f32_e32 v16, v16
	v_exp_f32_e32 v17, v17
	v_exp_f32_e32 v18, v18
	v_exp_f32_e32 v19, v19
	s_nop 0
	v_exp_f32_e32 v20, v20
	v_exp_f32_e32 v21, v21
	v_exp_f32_e32 v22, v22
	v_exp_f32_e32 v23, v23
	s_nop 0
	v_exp_f32_e32 v24, v24
	v_exp_f32_e32 v25, v25
	v_exp_f32_e32 v26, v26
	v_exp_f32_e32 v27, v27
	s_nop 0
	v_exp_f32_e32 v28, v28
	v_exp_f32_e32 v29, v29
	v_exp_f32_e32 v30, v30
	v_exp_f32_e32 v31, v31
	v_exp_f32_e32 v0, v0
	v_exp_f32_e32 v1, v1
	v_exp_f32_e32 v2, v2
	v_exp_f32_e32 v3, v3
	s_nop 0
	v_exp_f32_e32 v4, v4
	v_exp_f32_e32 v5, v5
	v_exp_f32_e32 v6, v6
	v_exp_f32_e32 v7, v7
	s_nop 0
	v_exp_f32_e32 v8, v8
	v_exp_f32_e32 v9, v9
	v_exp_f32_e32 v10, v10
	v_exp_f32_e32 v11, v11
	s_nop 0
	v_exp_f32_e32 v12, v12
	v_exp_f32_e32 v13, v13
	v_exp_f32_e32 v14, v14
	v_exp_f32_e32 v15, v15
	s_waitcnt lgkmcnt(0)
	v_mfma_f32_32x32x16_bf16 v[80:95], v[36:39], v[128:131], 0
	s_add_i32 s53, 0, 0x2000
	v_add_u32_e32 v50, s53, v50
	v_add3_u32 v172, v50, v49, v48
	v_add_f32_e32 v52, v16, v17
	v_add_f32_e32 v53, v18, v19
	v_add_f32_e32 v54, v20, v21
	v_add_f32_e32 v55, v22, v23
	v_add_f32_e32 v56, v24, v25
	v_add_f32_e32 v57, v26, v27
	v_add_f32_e32 v58, v28, v29
	v_add_f32_e32 v59, v30, v31
	v_cvt_pk_bf16_f32 v16, v16, v17
	v_cvt_pk_bf16_f32 v17, v18, v19
	v_cvt_pk_bf16_f32 v18, v20, v21
	v_cvt_pk_bf16_f32 v19, v22, v23
	ds_read_b64_tr_b16 v[36:37], v172 offset:0
	ds_read_b64_tr_b16 v[38:39], v172 offset:512
	ds_read_b64_tr_b16 v[48:49], v172 offset:4096
	v_mfma_f32_32x32x16_bf16 v[80:95], v[40:43], v[132:135], v[80:95]
	ds_read_b64_tr_b16 v[50:51], v172 offset:4608
	ds_read_b64_tr_b16 v[104:105], v172 offset:1024
	ds_read_b64_tr_b16 v[106:107], v172 offset:1536
	ds_read_b64_tr_b16 v[100:101], v172 offset:5120
	ds_read_b64_tr_b16 v[102:103], v172 offset:5632
	v_add_f32_e32 v20, v52, v53
	v_add_f32_e32 v21, v54, v55
	v_add_f32_e32 v22, v56, v57
	v_add_f32_e32 v23, v58, v59
	v_cvt_pk_bf16_f32 v108, v24, v25
	v_cvt_pk_bf16_f32 v109, v26, v27
	v_cvt_pk_bf16_f32 v110, v28, v29
	v_cvt_pk_bf16_f32 v111, v30, v31
	s_nop 0
	v_add_f32_e32 v20, v20, v21
	v_add_f32_e32 v21, v22, v23
	v_mfma_f32_32x32x16_bf16 v[64:79], v[44:47], v[136:139], 0
	v_add_f32_e32 v22, v0, v1
	v_add_f32_e32 v23, v2, v3
	v_add_f32_e32 v24, v4, v5
	v_add_f32_e32 v25, v6, v7
	v_add_f32_e32 v26, v8, v9
	v_add_f32_e32 v27, v10, v11
	v_add_f32_e32 v28, v12, v13
	v_add_f32_e32 v29, v14, v15
	v_cvt_pk_bf16_f32 v52, v0, v1
	v_cvt_pk_bf16_f32 v53, v2, v3
	v_cvt_pk_bf16_f32 v54, v4, v5
	v_cvt_pk_bf16_f32 v55, v6, v7
	v_add_f32_e32 v0, v20, v21
	v_mfma_f32_32x32x16_bf16 v[64:79], v[32:35], v[140:143], v[64:79]
	v_add_f32_e32 v1, v22, v23
	v_add_f32_e32 v2, v24, v25
	v_add_f32_e32 v3, v26, v27
	v_add_f32_e32 v4, v28, v29
	v_cvt_pk_bf16_f32 v112, v8, v9
	v_cvt_pk_bf16_f32 v113, v10, v11
	v_cvt_pk_bf16_f32 v114, v12, v13
	v_cvt_pk_bf16_f32 v115, v14, v15
	s_nop 0
	v_add_f32_e32 v1, v1, v2
	v_add_f32_e32 v2, v3, v4
	v_add_f32_e32 v174, v166, v0
	s_mov_b32 s60, 0
	v_add_f32_e32 v0, v1, v2
	s_waitcnt lgkmcnt(0)
	s_nop 0
	v_add_f32_e32 v175, v166, v0
	v_mfma_f32_32x32x16_bf16 v[0:15], v[16:19], v[36:39], 0
	ds_read_b128 v[96:99], v173 offset:16384
	ds_read_b128 v[152:155], v173 offset:18432
	ds_read_b128 v[148:151], v173 offset:20480
	ds_read_b128 v[144:147], v173 offset:22528
	s_nop 0
	v_exp_f32_e32 v80, v80
	v_exp_f32_e32 v81, v81
	v_exp_f32_e32 v82, v82
	v_exp_f32_e32 v83, v83
	v_mfma_f32_32x32x16_bf16 v[16:31], v[16:19], v[48:51], 0
	v_exp_f32_e32 v84, v84
	v_exp_f32_e32 v85, v85
	v_exp_f32_e32 v86, v86
	v_exp_f32_e32 v87, v87
	v_mfma_f32_32x32x16_bf16 v[32:47], v[52:55], v[36:39], 0
	v_exp_f32_e32 v88, v88
	v_exp_f32_e32 v89, v89
	v_exp_f32_e32 v90, v90
	v_exp_f32_e32 v91, v91
	v_mfma_f32_32x32x16_bf16 v[48:63], v[52:55], v[48:51], 0
	v_exp_f32_e32 v92, v92
	v_exp_f32_e32 v93, v93
	v_exp_f32_e32 v94, v94
	v_exp_f32_e32 v95, v95
	v_mfma_f32_32x32x16_bf16 v[0:15], v[108:111], v[104:107], v[0:15]
	v_exp_f32_e32 v64, v64
	v_exp_f32_e32 v65, v65
	v_exp_f32_e32 v66, v66
	v_exp_f32_e32 v67, v67
	v_mfma_f32_32x32x16_bf16 v[16:31], v[108:111], v[100:103], v[16:31]
	v_exp_f32_e32 v68, v68
	v_exp_f32_e32 v69, v69
	v_exp_f32_e32 v70, v70
	v_exp_f32_e32 v71, v71
	v_mfma_f32_32x32x16_bf16 v[32:47], v[112:115], v[104:107], v[32:47]
	v_exp_f32_e32 v72, v72
	v_exp_f32_e32 v73, v73
	v_exp_f32_e32 v74, v74
	v_exp_f32_e32 v75, v75
	v_mfma_f32_32x32x16_bf16 v[48:63], v[112:115], v[100:103], v[48:63]
	v_exp_f32_e32 v76, v76
	v_exp_f32_e32 v77, v77
	v_exp_f32_e32 v78, v78
	v_exp_f32_e32 v79, v79
	s_add_u32 s54, s30, s0
	v_add_u32_e32 v176, 0x800, v172
	s_addc_u32 s55, s31, s1
	s_mov_b32 s57, 0x10000
	s_movk_i32 s56, 0x4000
	s_mov_b64 s[0:1], 0
	s_cmpk_lt_i32 s95, 0x700
	s_cbranch_scc1 .Lswa_touch_skip
; #define ATT_WAITV(n) asm volatile("s_waitcnt vmcnt(" #n ")" ::: "memory")
; #define ATT_BAR() do { asm volatile("s_waitcnt lgkmcnt(0)" ::: "memory"); __builtin_amdgcn_s_barrier(); asm volatile("" ::: "memory"); } while (0)
; #define ATT_DMA(j, slot) ATT_DMA_S(S, j, slot)
; #define ATT_DMA(j, slot) ATT_DMA_S(S, j, slot)
; #define ATT_DMA(j, slot) ATT_DMA_S(S, j, slot)
; __device__ __forceinline__ void unit_diff(const P& p, LAS unsigned char* lds, const Src& S, float lam, bf16_t* orow, const int wid,
;                                           bf16x8 (&qr)[4], const bool pre  , const bool pn  , const Src& Sn) {
;     ...
;     for (int T = 1; T < NTR; ++T) {
;         if (T + 2 <= NTR) ATT_WAITV(2); else ATT_WAITV(0);
;         ATT_BAR();
;         if (T + 3 <= NTR) ATT_DMA(T + 3, sl_dma);
;         dstep<true, true>(A0, B0, A1, B1, kA, kB, lds + sl_cur + koff + 512, lbase + sl_prev + voff + 2048, qr, o1, o2, l1, l2);
;         dstep<true, true>(A1, B1, A0, B0, kB, kA, lds + sl_nxt + koff, lbase + sl_cur + voff, qr, o1, o2, l1, l2);
;         { const int f_ = sl_prev; sl_prev = sl_cur; sl_cur = sl_nxt; sl_nxt = sl_n2; sl_n2 = sl_dma; sl_dma = f_; }
;     }
	s_and_b32 s98, s95, 0xff
	v_readlane_b32 s100, v254, 5
	s_lshr_b32 s99, s98, 6
	s_lshr_b32 s100, s100, 4
	s_add_i32 s99, s99, s100
	s_lshl_b32 s99, s99, 19
	s_bfe_u32 s98, s98, 0x50001
	s_lshl_b32 s98, s98, 1
	s_add_i32 s98, s98, -2
	s_max_i32 s98, s98, 0
	s_lshl_b32 s98, s98, 13
	s_add_i32 s99, s99, s98
	s_add_u32 s100, s30, s99
	s_addc_u32 s101, s31, 0
	s_add_u32 s100, s100, 0xa000000
	s_addc_u32 s101, s101, 0
	v_mbcnt_lo_u32_b32 v213, -1, 0
	v_mbcnt_hi_u32_b32 v213, -1, v213
	v_lshlrev_b32_e32 v213, 7, v213
	global_load_dword v214, v213, s[100:101]
	s_add_u32 s100, s100, 0x2000
	s_addc_u32 s101, s101, 0
	global_load_dword v214, v213, s[100:101]
	s_add_u32 s100, s100, 0x2000
	s_addc_u32 s101, s101, 0
	global_load_dword v214, v213, s[100:101]
	s_add_u32 s100, s100, 0x2000
	s_addc_u32 s101, s101, 0
	global_load_dword v214, v213, s[100:101]
	s_add_u32 s100, s100, 0x2000
	s_addc_u32 s101, s101, 0
	global_load_dword v214, v213, s[100:101]
	s_add_u32 s100, s100, 0x2000
	s_addc_u32 s101, s101, 0
	global_load_dword v214, v213, s[100:101]
	s_add_u32 s100, s100, 0xff6000
	s_addc_u32 s101, s101, 0
	global_load_dword v214, v213, s[100:101]
	s_add_u32 s100, s100, 0x2000
	s_addc_u32 s101, s101, 0
	global_load_dword v214, v213, s[100:101]
	s_add_u32 s100, s100, 0x2000
	s_addc_u32 s101, s101, 0
	global_load_dword v214, v213, s[100:101]
	s_add_u32 s100, s100, 0x2000
	s_addc_u32 s101, s101, 0
	global_load_dword v214, v213, s[100:101]
	s_add_u32 s100, s100, 0x2000
	s_addc_u32 s101, s101, 0
	global_load_dword v214, v213, s[100:101]
	s_add_u32 s100, s100, 0x2000
	s_addc_u32 s101, s101, 0
	global_load_dword v214, v213, s[100:101]
.Lswa_touch_skip:
.LBB7_438:
	s_add_u32 s53, s54, s0
	s_addc_u32 s58, s55, s1
	s_add_u32 s61, s53, 0x10008000
	s_addc_u32 s62, s58, 0
	s_add_u32 s53, s53, 0x14008000
	s_addc_u32 s58, s58, 0
	s_cmp_eq_u32 s0, 0x78000
	s_waitcnt vmcnt(2)
	s_cselect_b32 s63, s11, s62
	s_cselect_b32 s62, s10, s61
	s_cselect_b32 s65, s36, s58
	s_cselect_b32 s64, s13, s53
	s_add_i32 s53, s41, s57
	s_waitcnt lgkmcnt(0)
	s_barrier
	v_lshl_add_u64 v[100:101], s[62:63], 0, v[160:161]
	s_mov_b32 m0, s53
	s_mov_b32 s58, s60
	global_load_lds_dwordx4 v[100:101], off
	v_lshl_add_u64 v[100:101], s[64:65], 0, v[160:161]
	s_add_i32 m0, s53, 0x2000
	s_mov_b32 s53, s59
	global_load_lds_dwordx4 v[100:101], off
	v_add_u32_e32 v177, s56, v173
	v_add_u32_e32 v100, s58, v176
	s_waitcnt lgkmcnt(0)
	v_mfma_f32_32x32x16_bf16 v[112:127], v[96:99], v[128:131], 0
	v_add_f32_e32 v96, v80, v81
	v_add_f32_e32 v97, v82, v83
	v_add_f32_e32 v98, v84, v85
	v_add_f32_e32 v99, v86, v87
	v_add_f32_e32 v101, v88, v89
	v_add_f32_e32 v102, v90, v91
	v_add_f32_e32 v103, v92, v93
	v_add_f32_e32 v104, v94, v95
	v_cvt_pk_bf16_f32 v178, v80, v81
	v_cvt_pk_bf16_f32 v179, v82, v83
	v_cvt_pk_bf16_f32 v180, v84, v85
	v_cvt_pk_bf16_f32 v181, v86, v87
	ds_read_b64_tr_b16 v[182:183], v100 offset:0
	ds_read_b64_tr_b16 v[184:185], v100 offset:512
	ds_read_b64_tr_b16 v[186:187], v100 offset:4096
	ds_read_b64_tr_b16 v[188:189], v100 offset:4608
	ds_read_b64_tr_b16 v[84:85], v100 offset:1024
	ds_read_b64_tr_b16 v[86:87], v100 offset:1536
	ds_read_b64_tr_b16 v[80:81], v100 offset:5120
	ds_read_b64_tr_b16 v[82:83], v100 offset:5632
	v_mfma_f32_32x32x16_bf16 v[112:127], v[152:155], v[132:135], v[112:127]
	v_add_f32_e32 v96, v96, v97
	v_add_f32_e32 v97, v98, v99
	v_add_f32_e32 v98, v101, v102
	v_add_f32_e32 v99, v103, v104
	v_cvt_pk_bf16_f32 v88, v88, v89
	v_cvt_pk_bf16_f32 v89, v90, v91
	v_cvt_pk_bf16_f32 v90, v92, v93
	v_cvt_pk_bf16_f32 v91, v94, v95
	s_nop 0
	v_add_f32_e32 v92, v96, v97
	v_add_f32_e32 v93, v98, v99
	v_mfma_f32_32x32x16_bf16 v[96:111], v[148:151], v[136:139], 0
	v_add_f32_e32 v94, v64, v65
	v_add_f32_e32 v95, v66, v67
	v_add_f32_e32 v148, v68, v69
	v_add_f32_e32 v149, v70, v71
	v_add_f32_e32 v150, v72, v73
	v_add_f32_e32 v151, v74, v75
	v_add_f32_e32 v152, v76, v77
	v_add_f32_e32 v153, v78, v79
	v_cvt_pk_bf16_f32 v64, v64, v65
	v_cvt_pk_bf16_f32 v65, v66, v67
	v_cvt_pk_bf16_f32 v66, v68, v69
	v_cvt_pk_bf16_f32 v67, v70, v71
	v_add_f32_e32 v92, v92, v93
	v_mfma_f32_32x32x16_bf16 v[96:111], v[144:147], v[140:143], v[96:111]
	v_add_f32_e32 v93, v94, v95
	v_add_f32_e32 v94, v148, v149
	v_add_f32_e32 v95, v150, v151
	v_add_f32_e32 v144, v152, v153
	v_cvt_pk_bf16_f32 v68, v72, v73
	v_cvt_pk_bf16_f32 v69, v74, v75
	v_cvt_pk_bf16_f32 v70, v76, v77
	v_cvt_pk_bf16_f32 v71, v78, v79
	s_nop 0
	v_add_f32_e32 v72, v93, v94
	v_add_f32_e32 v73, v95, v144
	v_add_f32_e32 v152, v174, v92
	s_nop 0
	v_add_f32_e32 v72, v72, v73
	s_waitcnt lgkmcnt(0)
	v_mfma_f32_32x32x16_bf16 v[0:15], v[178:181], v[182:185], v[0:15]
	v_add_f32_e32 v153, v175, v72
	ds_read_b128 v[72:75], v177 offset:512
	ds_read_b128 v[76:79], v177 offset:2560
	ds_read_b128 v[148:151], v177 offset:4608
	ds_read_b128 v[144:147], v177 offset:6656
	s_nop 1
	v_exp_f32_e32 v112, v112
	v_exp_f32_e32 v113, v113
	v_exp_f32_e32 v114, v114
	v_exp_f32_e32 v115, v115
	v_mfma_f32_32x32x16_bf16 v[16:31], v[178:181], v[186:189], v[16:31]
	v_exp_f32_e32 v116, v116
	v_exp_f32_e32 v117, v117
	v_exp_f32_e32 v118, v118
	v_exp_f32_e32 v119, v119
	v_mfma_f32_32x32x16_bf16 v[32:47], v[64:67], v[182:185], v[32:47]
	v_exp_f32_e32 v120, v120
	v_exp_f32_e32 v121, v121
	v_exp_f32_e32 v122, v122
	v_exp_f32_e32 v123, v123
	v_mfma_f32_32x32x16_bf16 v[48:63], v[64:67], v[186:189], v[48:63]
	v_exp_f32_e32 v124, v124
	v_exp_f32_e32 v125, v125
	v_exp_f32_e32 v126, v126
	v_exp_f32_e32 v127, v127
	v_mfma_f32_32x32x16_bf16 v[0:15], v[88:91], v[84:87], v[0:15]
	v_exp_f32_e32 v96, v96
	v_exp_f32_e32 v97, v97
	v_exp_f32_e32 v98, v98
	v_exp_f32_e32 v99, v99
	v_mfma_f32_32x32x16_bf16 v[16:31], v[88:91], v[80:83], v[16:31]
	v_exp_f32_e32 v100, v100
	v_exp_f32_e32 v101, v101
	v_exp_f32_e32 v102, v102
	v_exp_f32_e32 v103, v103
	v_mfma_f32_32x32x16_bf16 v[32:47], v[68:71], v[84:87], v[32:47]
	v_exp_f32_e32 v104, v104
	v_exp_f32_e32 v105, v105
	v_exp_f32_e32 v106, v106
	v_exp_f32_e32 v107, v107
	v_mfma_f32_32x32x16_bf16 v[48:63], v[68:71], v[80:83], v[48:63]
	v_exp_f32_e32 v108, v108
	v_exp_f32_e32 v109, v109
	v_exp_f32_e32 v110, v110
	v_exp_f32_e32 v111, v111
	s_waitcnt lgkmcnt(0)
; template <bool HAVE_PREV, bool HAVE_NEXT> __device__ __forceinline__ void dstep(f32x16& ca, f32x16& cb, f32x16& pa, f32x16& pb, const bf16x8 (&kf)[4], bf16x8 (&kn)[4], const LAS unsigned char* kbn, unsigned vpa, ...
;     const f32x16 z = {0.f, 0.f, 0.f, 0.f, 0.f, 0.f, 0.f, 0.f, 0.f, 0.f, 0.f, 0.f, 0.f, 0.f, 0.f, 0.f};
;     s16x4 vl[2][2], vh[2][2]; u32x4 wa[2], wb[2];
;     ca = __builtin_amdgcn_mfma_f32_32x32x16_bf16(kf[0], qr[0], z, 0, 0, 0);
;     float a0, a1, a2, a3, a4, a5, a6, a7, b0, b1, b2, b3, b4, b5, b6, b7;
;     if (HAVE_PREV) { a0 = fadd_s(pa[0], pa[1]); a1 = fadd_s(pa[2], pa[3]); a2 = fadd_s(pa[4], pa[5]); a3 = fadd_s(pa[6], pa[7]); a4 = fadd_s(pa[8], pa[9]); a5 = fadd_s(pa[10], pa[11]); a6 = fadd_s(pa[12], pa[13]); a7 = fadd_s(pa[14], pa[15]);
;         wa[0].x = cvtpk(pa[0], pa[1]); wa[0].y = cvtpk(pa[2], pa[3]); wa[0].z = cvtpk(pa[4], pa[5]); wa[0].w = cvtpk(pa[6], pa[7]); }
;     ATT_SB();
;     ca = __builtin_amdgcn_mfma_f32_32x32x16_bf16(kf[1], qr[1], ca, 0, 0, 0);
;     if (HAVE_PREV) {
;         ATT_TR(vl[0][0], vpa, 0); ATT_TR(vh[0][0], vpa, 512); ATT_TR(vl[1][0], vpa, 4096); ATT_TR(vh[1][0], vpa, 4096 + 512);
;         ATT_TR(vl[0][1], vpa, 1024); ATT_TR(vh[0][1], vpa, 1024 + 512); ATT_TR(vl[1][1], vpa, 4096 + 1024); ATT_TR(vh[1][1], vpa, 4096 + 1024 + 512);
;         a0 = fadd_s(a0, a1); a2 = fadd_s(a2, a3); a4 = fadd_s(a4, a5); a6 = fadd_s(a6, a7);
;         wa[1].x = cvtpk(pa[8], pa[9]); wa[1].y = cvtpk(pa[10], pa[11]); wa[1].z = cvtpk(pa[12], pa[13]); wa[1].w = cvtpk(pa[14], pa[15]);
;         a0 = fadd_s(a0, a2); a4 = fadd_s(a4, a6); }
; __device__ __forceinline__ void unit_diff(const P& p, LAS unsigned char* lds, const Src& S, float lam, bf16_t* orow, const int wid,
;                                           bf16x8 (&qr)[4], const bool pre  , const bool pn  , const Src& Sn) {
;     ...
;     for (int T = 1; T < NTR; ++T) {
;         if (T + 2 <= NTR) ATT_WAITV(2); else ATT_WAITV(0);
;         ATT_BAR();
;         if (T + 3 <= NTR) ATT_DMA(T + 3, sl_dma);
;         dstep<true, true>(A0, B0, A1, B1, kA, kB, lds + sl_cur + koff + 512, lbase + sl_prev + voff + 2048, qr, o1, o2, l1, l2);
;         dstep<true, true>(A1, B1, A0, B0, kB, kA, lds + sl_nxt + koff, lbase + sl_cur + voff, qr, o1, o2, l1, l2);
;         { const int f_ = sl_prev; sl_prev = sl_cur; sl_cur = sl_nxt; sl_nxt = sl_n2; sl_n2 = sl_dma; sl_dma = f_; }
;     }
	v_mfma_f32_32x32x16_bf16 v[80:95], v[72:75], v[128:131], 0
	v_add_u32_e32 v64, s56, v172
	v_add_u32_e32 v177, s53, v173
	v_add_f32_e32 v65, v112, v113
	v_add_f32_e32 v66, v114, v115
	v_add_f32_e32 v67, v116, v117
	v_add_f32_e32 v68, v118, v119
	v_add_f32_e32 v69, v120, v121
	v_add_f32_e32 v70, v122, v123
	v_add_f32_e32 v71, v124, v125
	v_add_f32_e32 v72, v126, v127
	v_cvt_pk_bf16_f32 v178, v112, v113
	v_cvt_pk_bf16_f32 v179, v114, v115
	v_cvt_pk_bf16_f32 v180, v116, v117
	v_cvt_pk_bf16_f32 v181, v118, v119
	ds_read_b64_tr_b16 v[182:183], v64 offset:0
	ds_read_b64_tr_b16 v[184:185], v64 offset:512
	ds_read_b64_tr_b16 v[186:187], v64 offset:4096
	v_mfma_f32_32x32x16_bf16 v[80:95], v[76:79], v[132:135], v[80:95]
	ds_read_b64_tr_b16 v[188:189], v64 offset:4608
	ds_read_b64_tr_b16 v[116:117], v64 offset:1024
	ds_read_b64_tr_b16 v[118:119], v64 offset:1536
	ds_read_b64_tr_b16 v[112:113], v64 offset:5120
	ds_read_b64_tr_b16 v[114:115], v64 offset:5632
	v_add_f32_e32 v64, v65, v66
	v_add_f32_e32 v65, v67, v68
	v_add_f32_e32 v66, v69, v70
	v_add_f32_e32 v67, v71, v72
	v_cvt_pk_bf16_f32 v120, v120, v121
	v_cvt_pk_bf16_f32 v121, v122, v123
	v_cvt_pk_bf16_f32 v122, v124, v125
	v_cvt_pk_bf16_f32 v123, v126, v127
	s_nop 0
	v_add_f32_e32 v154, v64, v65
	v_add_f32_e32 v155, v66, v67
	v_mfma_f32_32x32x16_bf16 v[64:79], v[148:151], v[136:139], 0
	v_add_f32_e32 v148, v96, v97
	v_add_f32_e32 v149, v98, v99
	v_add_f32_e32 v150, v100, v101
	v_add_f32_e32 v151, v102, v103
	v_add_f32_e32 v174, v104, v105
	v_add_f32_e32 v175, v106, v107
	v_add_f32_e32 v190, v108, v109
	v_add_f32_e32 v191, v110, v111
	v_cvt_pk_bf16_f32 v124, v96, v97
	v_cvt_pk_bf16_f32 v125, v98, v99
	v_cvt_pk_bf16_f32 v126, v100, v101
	v_cvt_pk_bf16_f32 v127, v102, v103
	v_add_f32_e32 v96, v154, v155
	v_mfma_f32_32x32x16_bf16 v[64:79], v[144:147], v[140:143], v[64:79]
	v_add_f32_e32 v97, v148, v149
	v_add_f32_e32 v98, v150, v151
	v_add_f32_e32 v99, v174, v175
	v_add_f32_e32 v144, v190, v191
	v_cvt_pk_bf16_f32 v100, v104, v105
	v_cvt_pk_bf16_f32 v101, v106, v107
	v_cvt_pk_bf16_f32 v102, v108, v109
	v_cvt_pk_bf16_f32 v103, v110, v111
	s_nop 0
	v_add_f32_e32 v97, v97, v98
	v_add_f32_e32 v98, v99, v144
	v_add_f32_e32 v174, v152, v96
	s_nop 0
	v_add_f32_e32 v96, v97, v98
	s_waitcnt lgkmcnt(0)
	v_mfma_f32_32x32x16_bf16 v[0:15], v[178:181], v[182:185], v[0:15]
	v_add_f32_e32 v175, v153, v96
	ds_read_b128 v[96:99], v177
	ds_read_b128 v[152:155], v177 offset:2048
	ds_read_b128 v[148:151], v177 offset:4096
	ds_read_b128 v[144:147], v177 offset:6144
	s_nop 1
	v_exp_f32_e32 v80, v80
	v_exp_f32_e32 v81, v81
	v_exp_f32_e32 v82, v82
	v_exp_f32_e32 v83, v83
	v_mfma_f32_32x32x16_bf16 v[16:31], v[178:181], v[186:189], v[16:31]
	v_exp_f32_e32 v84, v84
	v_exp_f32_e32 v85, v85
	v_exp_f32_e32 v86, v86
	v_exp_f32_e32 v87, v87
	v_mfma_f32_32x32x16_bf16 v[32:47], v[124:127], v[182:185], v[32:47]
	v_exp_f32_e32 v88, v88
	v_exp_f32_e32 v89, v89
	v_exp_f32_e32 v90, v90
	v_exp_f32_e32 v91, v91
	v_mfma_f32_32x32x16_bf16 v[48:63], v[124:127], v[186:189], v[48:63]
	v_exp_f32_e32 v92, v92
	v_exp_f32_e32 v93, v93
	v_exp_f32_e32 v94, v94
	v_exp_f32_e32 v95, v95
	v_mfma_f32_32x32x16_bf16 v[0:15], v[120:123], v[116:119], v[0:15]
	v_exp_f32_e32 v64, v64
	v_exp_f32_e32 v65, v65
	v_exp_f32_e32 v66, v66
	v_exp_f32_e32 v67, v67
	v_mfma_f32_32x32x16_bf16 v[16:31], v[120:123], v[112:115], v[16:31]
	v_exp_f32_e32 v68, v68
	v_exp_f32_e32 v69, v69
	v_exp_f32_e32 v70, v70
	v_exp_f32_e32 v71, v71
	v_mfma_f32_32x32x16_bf16 v[32:47], v[100:103], v[116:119], v[32:47]
	v_exp_f32_e32 v72, v72
	v_exp_f32_e32 v73, v73
	v_exp_f32_e32 v74, v74
	v_exp_f32_e32 v75, v75
	v_mfma_f32_32x32x16_bf16 v[48:63], v[100:103], v[112:115], v[48:63]
	v_exp_f32_e32 v76, v76
	v_exp_f32_e32 v77, v77
	v_exp_f32_e32 v78, v78
	v_exp_f32_e32 v79, v79
	s_add_u32 s0, s0, 0x2000
	s_addc_u32 s1, s1, 0
	s_mov_b32 s60, s56
	s_mov_b32 s56, s59
	s_mov_b32 s59, s37
	s_mov_b32 s37, s57
	s_cmp_eq_u32 s0, 0x7a000
	s_mov_b32 s57, s58
	s_cbranch_scc0 .LBB7_438
	s_waitcnt lgkmcnt(0)
	v_mfma_f32_32x32x16_bf16 v[96:111], v[96:99], v[128:131], 0
	s_add_i32 s83, s83, 1
	s_add_i32 s60, s95, s3
	s_cmpk_gt_i32 s60, 0x7ff
	s_cselect_b64 s[0:1], -1, 0
	s_cmpk_lt_i32 s60, 0x800
	s_waitcnt vmcnt(2)
	s_cselect_b64 s[10:11], -1, 0
	s_cmp_lg_u32 s83, s78
	s_waitcnt lgkmcnt(0)
	s_barrier
; template <bool HAVE_PREV, bool HAVE_NEXT> __device__ __forceinline__ void dstep(f32x16& ca, f32x16& cb, f32x16& pa, f32x16& pb, const bf16x8 (&kf)[4], bf16x8 (&kn)[4], const LAS unsigned char* kbn, unsigned vpa, ...
;     const f32x16 z = {0.f, 0.f, 0.f, 0.f, 0.f, 0.f, 0.f, 0.f, 0.f, 0.f, 0.f, 0.f, 0.f, 0.f, 0.f, 0.f};
;     s16x4 vl[2][2], vh[2][2]; u32x4 wa[2], wb[2];
;     ca = __builtin_amdgcn_mfma_f32_32x32x16_bf16(kf[0], qr[0], z, 0, 0, 0);
;     float a0, a1, a2, a3, a4, a5, a6, a7, b0, b1, b2, b3, b4, b5, b6, b7;
;     if (HAVE_PREV) { a0 = fadd_s(pa[0], pa[1]); a1 = fadd_s(pa[2], pa[3]); a2 = fadd_s(pa[4], pa[5]); a3 = fadd_s(pa[6], pa[7]); a4 = fadd_s(pa[8], pa[9]); a5 = fadd_s(pa[10], pa[11]); a6 = fadd_s(pa[12], pa[13]); a7 = fadd_s(pa[14], pa[15]);
;         wa[0].x = cvtpk(pa[0], pa[1]); wa[0].y = cvtpk(pa[2], pa[3]); wa[0].z = cvtpk(pa[4], pa[5]); wa[0].w = cvtpk(pa[6], pa[7]); }
;     ATT_SB();
;     ca = __builtin_amdgcn_mfma_f32_32x32x16_bf16(kf[1], qr[1], ca, 0, 0, 0);
;     if (HAVE_PREV) {
;         ATT_TR(vl[0][0], vpa, 0); ATT_TR(vh[0][0], vpa, 512); ATT_TR(vl[1][0], vpa, 4096); ATT_TR(vh[1][0], vpa, 4096 + 512);
;         ATT_TR(vl[0][1], vpa, 1024); ATT_TR(vh[0][1], vpa, 1024 + 512); ATT_TR(vl[1][1], vpa, 4096 + 1024); ATT_TR(vh[1][1], vpa, 4096 + 1024 + 512);
;         a0 = fadd_s(a0, a1); a2 = fadd_s(a2, a3); a4 = fadd_s(a4, a5); a6 = fadd_s(a6, a7);
;         wa[1].x = cvtpk(pa[8], pa[9]); wa[1].y = cvtpk(pa[10], pa[11]); wa[1].z = cvtpk(pa[12], pa[13]); wa[1].w = cvtpk(pa[14], pa[15]);
;         a0 = fadd_s(a0, a2); a4 = fadd_s(a4, a6); }
; __device__ __forceinline__ void unit_diff(const P& p, LAS unsigned char* lds, const Src& S, float lam, bf16_t* orow, const int wid,
;                                           bf16x8 (&qr)[4], const bool pre  , const bool pn  , const Src& Sn) {
;     ...
;     for (int T = 1; T < NTR; ++T) {
;         if (T + 2 <= NTR) ATT_WAITV(2); else ATT_WAITV(0);
;         ATT_BAR();
;         if (T + 3 <= NTR) ATT_DMA(T + 3, sl_dma);
;         dstep<true, true>(A0, B0, A1, B1, kA, kB, lds + sl_cur + koff + 512, lbase + sl_prev + voff + 2048, qr, o1, o2, l1, l2);
;         dstep<true, true>(A1, B1, A0, B0, kB, kA, lds + sl_nxt + koff, lbase + sl_cur + voff, qr, o1, o2, l1, l2);
;         { const int f_ = sl_prev; sl_prev = sl_cur; sl_cur = sl_nxt; sl_nxt = sl_n2; sl_n2 = sl_dma; sl_dma = f_; }
;     }
	s_cselect_b64 s[54:55], -1, 0
	s_and_b64 s[56:57], s[10:11], s[54:55]
	v_add_u32_e32 v180, 0x4800, v172
	v_add_f32_e32 v181, v80, v81
	v_add_f32_e32 v182, v82, v83
	v_add_f32_e32 v183, v84, v85
	v_add_f32_e32 v184, v86, v87
	v_add_f32_e32 v185, v88, v89
	v_add_f32_e32 v186, v90, v91
	v_add_f32_e32 v187, v92, v93
	v_add_f32_e32 v188, v94, v95
	v_cvt_pk_bf16_f32 v120, v80, v81
	v_cvt_pk_bf16_f32 v121, v82, v83
	v_cvt_pk_bf16_f32 v122, v84, v85
	v_cvt_pk_bf16_f32 v123, v86, v87
	ds_read_b64_tr_b16 v[124:125], v180 offset:0
	ds_read_b64_tr_b16 v[126:127], v180 offset:512
	ds_read_b64_tr_b16 v[176:177], v180 offset:4096
	v_mfma_f32_32x32x16_bf16 v[96:111], v[152:155], v[132:135], v[96:111]
	ds_read_b64_tr_b16 v[178:179], v180 offset:4608
	ds_read_b64_tr_b16 v[116:117], v180 offset:1024
	ds_read_b64_tr_b16 v[118:119], v180 offset:1536
	ds_read_b64_tr_b16 v[112:113], v180 offset:5120
	ds_read_b64_tr_b16 v[114:115], v180 offset:5632
	v_add_f32_e32 v80, v181, v182
	v_add_f32_e32 v81, v183, v184
	v_add_f32_e32 v82, v185, v186
	v_add_f32_e32 v83, v187, v188
	v_cvt_pk_bf16_f32 v152, v88, v89
	v_cvt_pk_bf16_f32 v153, v90, v91
	v_cvt_pk_bf16_f32 v154, v92, v93
	v_cvt_pk_bf16_f32 v155, v94, v95
	s_nop 0
	v_add_f32_e32 v180, v80, v81
	v_add_f32_e32 v181, v82, v83
	v_mfma_f32_32x32x16_bf16 v[80:95], v[148:151], v[136:139], 0
	v_add_f32_e32 v148, v64, v65
	v_add_f32_e32 v149, v66, v67
	v_add_f32_e32 v150, v68, v69
	v_add_f32_e32 v151, v70, v71
	v_add_f32_e32 v182, v72, v73
	v_add_f32_e32 v183, v74, v75
	v_add_f32_e32 v184, v76, v77
	v_add_f32_e32 v185, v78, v79
	v_cvt_pk_bf16_f32 v64, v64, v65
	v_cvt_pk_bf16_f32 v65, v66, v67
	v_cvt_pk_bf16_f32 v66, v68, v69
	v_cvt_pk_bf16_f32 v67, v70, v71
	v_add_f32_e32 v180, v180, v181
	v_mfma_f32_32x32x16_bf16 v[80:95], v[144:147], v[140:143], v[80:95]
	v_add_f32_e32 v144, v148, v149
	v_add_f32_e32 v145, v150, v151
	v_add_f32_e32 v146, v182, v183
	v_add_f32_e32 v147, v184, v185
	v_cvt_pk_bf16_f32 v68, v72, v73
	v_cvt_pk_bf16_f32 v69, v74, v75
	v_cvt_pk_bf16_f32 v70, v76, v77
	v_cvt_pk_bf16_f32 v71, v78, v79
	s_nop 0
	v_add_f32_e32 v72, v144, v145
	v_add_f32_e32 v73, v146, v147
	v_add_f32_e32 v182, v174, v180
	s_nop 0
	v_add_f32_e32 v72, v72, v73
	s_waitcnt lgkmcnt(0)
	v_add_u32_e32 v144, s53, v173
	v_mfma_f32_32x32x16_bf16 v[0:15], v[120:123], v[124:127], v[0:15]
	v_add_f32_e32 v183, v175, v72
	ds_read_b128 v[72:75], v144 offset:512
	ds_read_b128 v[76:79], v144 offset:2560
	ds_read_b128 v[148:151], v144 offset:4608
	ds_read_b128 v[144:147], v144 offset:6656
	s_nop 0
	v_exp_f32_e32 v96, v96
	v_exp_f32_e32 v97, v97
	v_exp_f32_e32 v98, v98
	v_exp_f32_e32 v99, v99
	v_mfma_f32_32x32x16_bf16 v[16:31], v[120:123], v[176:179], v[16:31]
	v_exp_f32_e32 v100, v100
	v_exp_f32_e32 v101, v101
	v_exp_f32_e32 v102, v102
	v_exp_f32_e32 v103, v103
	v_mfma_f32_32x32x16_bf16 v[32:47], v[64:67], v[124:127], v[32:47]
	v_exp_f32_e32 v104, v104
	v_exp_f32_e32 v105, v105
	v_exp_f32_e32 v106, v106
	v_exp_f32_e32 v107, v107
	v_mfma_f32_32x32x16_bf16 v[48:63], v[64:67], v[176:179], v[48:63]
	v_exp_f32_e32 v108, v108
	v_exp_f32_e32 v109, v109
	v_exp_f32_e32 v110, v110
	v_exp_f32_e32 v111, v111
	v_mfma_f32_32x32x16_bf16 v[0:15], v[152:155], v[116:119], v[0:15]
	v_exp_f32_e32 v80, v80
	v_exp_f32_e32 v81, v81
	v_exp_f32_e32 v82, v82
	v_exp_f32_e32 v83, v83
	v_mfma_f32_32x32x16_bf16 v[16:31], v[152:155], v[112:115], v[16:31]
	v_exp_f32_e32 v84, v84
	v_exp_f32_e32 v85, v85
	v_exp_f32_e32 v86, v86
	v_exp_f32_e32 v87, v87
	v_mfma_f32_32x32x16_bf16 v[32:47], v[68:71], v[116:119], v[32:47]
	v_exp_f32_e32 v88, v88
	v_exp_f32_e32 v89, v89
	v_exp_f32_e32 v90, v90
	v_exp_f32_e32 v91, v91
	v_mfma_f32_32x32x16_bf16 v[48:63], v[68:71], v[112:115], v[48:63]
	v_exp_f32_e32 v92, v92
	v_exp_f32_e32 v93, v93
	v_exp_f32_e32 v94, v94
	v_exp_f32_e32 v95, v95
	v_add_u32_e32 v64, 0x8000, v172
	v_add_f32_e32 v65, v96, v97
	v_add_f32_e32 v66, v98, v99
	v_add_f32_e32 v67, v100, v101
	v_add_f32_e32 v68, v102, v103
	v_add_f32_e32 v69, v104, v105
	s_waitcnt lgkmcnt(0)
	v_mfma_f32_32x32x16_bf16 v[112:127], v[72:75], v[128:131], 0
	v_add_f32_e32 v70, v106, v107
	v_add_f32_e32 v71, v108, v109
	v_add_f32_e32 v72, v110, v111
	v_cvt_pk_bf16_f32 v152, v96, v97
	v_cvt_pk_bf16_f32 v153, v98, v99
	v_cvt_pk_bf16_f32 v154, v100, v101
	v_cvt_pk_bf16_f32 v155, v102, v103
	ds_read_b64_tr_b16 v[174:175], v64 offset:0
	ds_read_b64_tr_b16 v[176:177], v64 offset:512
	ds_read_b64_tr_b16 v[178:179], v64 offset:4096
	ds_read_b64_tr_b16 v[180:181], v64 offset:4608
	ds_read_b64_tr_b16 v[100:101], v64 offset:1024
	ds_read_b64_tr_b16 v[102:103], v64 offset:1536
	ds_read_b64_tr_b16 v[96:97], v64 offset:5120
	ds_read_b64_tr_b16 v[98:99], v64 offset:5632
	v_mfma_f32_32x32x16_bf16 v[112:127], v[76:79], v[132:135], v[112:127]
	v_add_f32_e32 v64, v65, v66
	v_add_f32_e32 v65, v67, v68
	v_add_f32_e32 v66, v69, v70
	v_add_f32_e32 v67, v71, v72
	v_cvt_pk_bf16_f32 v104, v104, v105
	v_cvt_pk_bf16_f32 v105, v106, v107
	v_cvt_pk_bf16_f32 v106, v108, v109
	v_cvt_pk_bf16_f32 v107, v110, v111
	s_nop 0
	v_add_f32_e32 v108, v64, v65
	v_add_f32_e32 v109, v66, v67
	v_mfma_f32_32x32x16_bf16 v[64:79], v[148:151], v[136:139], 0
	v_add_f32_e32 v110, v80, v81
	v_add_f32_e32 v111, v82, v83
	v_add_f32_e32 v148, v84, v85
	v_add_f32_e32 v149, v86, v87
	v_add_f32_e32 v150, v88, v89
	v_add_f32_e32 v151, v90, v91
	v_add_f32_e32 v184, v92, v93
	v_add_f32_e32 v185, v94, v95
	v_cvt_pk_bf16_f32 v80, v80, v81
	v_cvt_pk_bf16_f32 v81, v82, v83
	v_cvt_pk_bf16_f32 v82, v84, v85
	v_cvt_pk_bf16_f32 v83, v86, v87
	v_add_f32_e32 v108, v108, v109
	v_mfma_f32_32x32x16_bf16 v[64:79], v[144:147], v[140:143], v[64:79]
	v_add_f32_e32 v109, v110, v111
	v_add_f32_e32 v110, v148, v149
	v_add_f32_e32 v111, v150, v151
	v_add_f32_e32 v144, v184, v185
	v_cvt_pk_bf16_f32 v84, v88, v89
	v_cvt_pk_bf16_f32 v85, v90, v91
	v_cvt_pk_bf16_f32 v86, v92, v93
	v_cvt_pk_bf16_f32 v87, v94, v95
	s_nop 0
	v_add_f32_e32 v88, v109, v110
	v_add_f32_e32 v89, v111, v144
	v_add_f32_e32 v182, v182, v108
	s_nop 0
	v_add_f32_e32 v88, v88, v89
	s_waitcnt lgkmcnt(0)
; #define LAS __attribute__((address_space(3)))
; template <bool HAVE_PREV, bool HAVE_NEXT> __device__ __forceinline__ void dstep(f32x16& ca, f32x16& cb, f32x16& pa, f32x16& pb, const bf16x8 (&kf)[4], bf16x8 (&kn)[4], const LAS unsigned char* kbn, unsigned vpa, ...
;     const f32x16 z = {0.f, 0.f, 0.f, 0.f, 0.f, 0.f, 0.f, 0.f, 0.f, 0.f, 0.f, 0.f, 0.f, 0.f, 0.f, 0.f};
;     s16x4 vl[2][2], vh[2][2]; u32x4 wa[2], wb[2];
;     ca = __builtin_amdgcn_mfma_f32_32x32x16_bf16(kf[0], qr[0], z, 0, 0, 0);
;     float a0, a1, a2, a3, a4, a5, a6, a7, b0, b1, b2, b3, b4, b5, b6, b7;
;     if (HAVE_PREV) { a0 = fadd_s(pa[0], pa[1]); a1 = fadd_s(pa[2], pa[3]); a2 = fadd_s(pa[4], pa[5]); a3 = fadd_s(pa[6], pa[7]); a4 = fadd_s(pa[8], pa[9]); a5 = fadd_s(pa[10], pa[11]); a6 = fadd_s(pa[12], pa[13]); a7 = fadd_s(pa[14], pa[15]);
;         wa[0].x = cvtpk(pa[0], pa[1]); wa[0].y = cvtpk(pa[2], pa[3]); wa[0].z = cvtpk(pa[4], pa[5]); wa[0].w = cvtpk(pa[6], pa[7]); }
;     ATT_SB();
;     ca = __builtin_amdgcn_mfma_f32_32x32x16_bf16(kf[1], qr[1], ca, 0, 0, 0);
;     if (HAVE_PREV) {
;         ATT_TR(vl[0][0], vpa, 0); ATT_TR(vh[0][0], vpa, 512); ATT_TR(vl[1][0], vpa, 4096); ATT_TR(vh[1][0], vpa, 4096 + 512);
;         ATT_TR(vl[0][1], vpa, 1024); ATT_TR(vh[0][1], vpa, 1024 + 512); ATT_TR(vl[1][1], vpa, 4096 + 1024); ATT_TR(vh[1][1], vpa, 4096 + 1024 + 512);
;         a0 = fadd_s(a0, a1); a2 = fadd_s(a2, a3); a4 = fadd_s(a4, a5); a6 = fadd_s(a6, a7);
; __device__ __forceinline__ void unit_diff(const P& p, LAS unsigned char* lds, const Src& S, float lam, bf16_t* orow, const int wid,
;                                           bf16x8 (&qr)[4], const bool pre  , const bool pn  , const Src& Sn) {
;     ...
;     for (int T = 1; T < NTR; ++T) {
;         if (T + 2 <= NTR) ATT_WAITV(2); else ATT_WAITV(0);
;         ATT_BAR();
;         if (T + 3 <= NTR) ATT_DMA(T + 3, sl_dma);
;         dstep<true, true>(A0, B0, A1, B1, kA, kB, lds + sl_cur + koff + 512, lbase + sl_prev + voff + 2048, qr, o1, o2, l1, l2);
;         dstep<true, true>(A1, B1, A0, B0, kB, kA, lds + sl_nxt + koff, lbase + sl_cur + voff, qr, o1, o2, l1, l2);
;         { const int f_ = sl_prev; sl_prev = sl_cur; sl_cur = sl_nxt; sl_nxt = sl_n2; sl_n2 = sl_dma; sl_dma = f_; }
;     }
;     ATT_WAITV(0); ATT_BAR();
;     dstep<true, false>(A0, B0, A1, B1, kA, kB, lds, lbase + sl_prev + voff + 2048, qr, o1, o2, l1, l2);
	v_mfma_f32_32x32x16_bf16 v[0:15], v[152:155], v[174:177], v[0:15]
	v_add_f32_e32 v183, v183, v88
	ds_read_b128 v[88:91], v173 offset:49152
	ds_read_b128 v[92:95], v173 offset:51200
	ds_read_b128 v[148:151], v173 offset:53248
	ds_read_b128 v[144:147], v173 offset:55296
	s_nop 1
	v_exp_f32_e32 v112, v112
	v_exp_f32_e32 v113, v113
	v_exp_f32_e32 v114, v114
	v_exp_f32_e32 v115, v115
	v_mfma_f32_32x32x16_bf16 v[16:31], v[152:155], v[178:181], v[16:31]
	v_exp_f32_e32 v116, v116
	v_exp_f32_e32 v117, v117
	v_exp_f32_e32 v118, v118
	v_exp_f32_e32 v119, v119
	v_mfma_f32_32x32x16_bf16 v[32:47], v[80:83], v[174:177], v[32:47]
	v_exp_f32_e32 v120, v120
	v_exp_f32_e32 v121, v121
	v_exp_f32_e32 v122, v122
	v_exp_f32_e32 v123, v123
	v_mfma_f32_32x32x16_bf16 v[48:63], v[80:83], v[178:181], v[48:63]
	v_exp_f32_e32 v124, v124
	v_exp_f32_e32 v125, v125
	v_exp_f32_e32 v126, v126
	v_exp_f32_e32 v127, v127
	v_mfma_f32_32x32x16_bf16 v[0:15], v[104:107], v[100:103], v[0:15]
	v_exp_f32_e32 v64, v64
	v_exp_f32_e32 v65, v65
	v_exp_f32_e32 v66, v66
	v_exp_f32_e32 v67, v67
	v_mfma_f32_32x32x16_bf16 v[16:31], v[104:107], v[96:99], v[16:31]
	v_exp_f32_e32 v68, v68
	v_exp_f32_e32 v69, v69
	v_exp_f32_e32 v70, v70
	v_exp_f32_e32 v71, v71
	v_mfma_f32_32x32x16_bf16 v[32:47], v[84:87], v[100:103], v[32:47]
	v_exp_f32_e32 v72, v72
	v_exp_f32_e32 v73, v73
	v_exp_f32_e32 v74, v74
	v_exp_f32_e32 v75, v75
	v_mfma_f32_32x32x16_bf16 v[48:63], v[84:87], v[96:99], v[48:63]
	v_exp_f32_e32 v76, v76
	v_exp_f32_e32 v77, v77
	v_exp_f32_e32 v78, v78
	v_exp_f32_e32 v79, v79
	s_waitcnt lgkmcnt(0)
	v_mfma_f32_32x32x16_bf16 v[96:111], v[88:91], v[128:131], 0
	s_waitcnt vmcnt(0)
	s_waitcnt lgkmcnt(0)
	s_barrier
	v_add_u32_e32 v80, 0x8800, v172
	v_add_f32_e32 v81, v112, v113
	v_add_f32_e32 v82, v114, v115
	v_add_f32_e32 v83, v116, v117
	v_add_f32_e32 v84, v118, v119
	v_add_f32_e32 v85, v120, v121
	v_add_f32_e32 v86, v122, v123
	v_add_f32_e32 v87, v124, v125
	v_add_f32_e32 v88, v126, v127
	v_cvt_pk_bf16_f32 v152, v112, v113
	v_cvt_pk_bf16_f32 v153, v114, v115
	v_cvt_pk_bf16_f32 v154, v116, v117
	v_cvt_pk_bf16_f32 v155, v118, v119
	ds_read_b64_tr_b16 v[174:175], v80 offset:0
	ds_read_b64_tr_b16 v[176:177], v80 offset:512
	ds_read_b64_tr_b16 v[178:179], v80 offset:4096
	v_mfma_f32_32x32x16_bf16 v[96:111], v[92:95], v[132:135], v[96:111]
	ds_read_b64_tr_b16 v[180:181], v80 offset:4608
	ds_read_b64_tr_b16 v[116:117], v80 offset:1024
	ds_read_b64_tr_b16 v[118:119], v80 offset:1536
	ds_read_b64_tr_b16 v[112:113], v80 offset:5120
	ds_read_b64_tr_b16 v[114:115], v80 offset:5632
	v_add_f32_e32 v80, v81, v82
	v_add_f32_e32 v81, v83, v84
	v_add_f32_e32 v82, v85, v86
	v_add_f32_e32 v83, v87, v88
	v_cvt_pk_bf16_f32 v120, v120, v121
	v_cvt_pk_bf16_f32 v121, v122, v123
	v_cvt_pk_bf16_f32 v122, v124, v125
	v_cvt_pk_bf16_f32 v123, v126, v127
	s_nop 0
	v_add_f32_e32 v184, v80, v81
	v_add_f32_e32 v185, v82, v83
	v_mfma_f32_32x32x16_bf16 v[80:95], v[148:151], v[136:139], 0
	v_add_f32_e32 v148, v64, v65
	v_add_f32_e32 v149, v66, v67
	v_add_f32_e32 v150, v68, v69
	v_add_f32_e32 v151, v70, v71
	v_add_f32_e32 v186, v72, v73
	v_add_f32_e32 v187, v74, v75
	v_add_f32_e32 v188, v76, v77
	v_add_f32_e32 v189, v78, v79
	v_cvt_pk_bf16_f32 v124, v64, v65
	v_cvt_pk_bf16_f32 v125, v66, v67
	v_cvt_pk_bf16_f32 v126, v68, v69
	v_cvt_pk_bf16_f32 v127, v70, v71
	v_add_f32_e32 v64, v184, v185
	v_mfma_f32_32x32x16_bf16 v[80:95], v[144:147], v[140:143], v[80:95]
	v_add_f32_e32 v65, v148, v149
	v_add_f32_e32 v66, v150, v151
	v_add_f32_e32 v67, v186, v187
	v_add_f32_e32 v144, v188, v189
	v_cvt_pk_bf16_f32 v68, v72, v73
	v_cvt_pk_bf16_f32 v69, v74, v75
	v_cvt_pk_bf16_f32 v70, v76, v77
	v_cvt_pk_bf16_f32 v71, v78, v79
	s_nop 0
	v_add_f32_e32 v65, v65, v66
	v_add_f32_e32 v66, v67, v144
	v_add_f32_e32 v182, v182, v64
	s_nop 0
	v_add_f32_e32 v64, v65, v66
	s_waitcnt lgkmcnt(0)
	v_mfma_f32_32x32x16_bf16 v[0:15], v[152:155], v[174:177], v[0:15]
	v_add_f32_e32 v183, v183, v64
	ds_read_b128 v[72:75], v173 offset:49664
	ds_read_b128 v[76:79], v173 offset:51712
	ds_read_b128 v[144:147], v173 offset:53760
	ds_read_b128 v[64:67], v173 offset:55808
	s_nop 1
	v_exp_f32_e32 v96, v96
	v_exp_f32_e32 v97, v97
	v_exp_f32_e32 v98, v98
	v_exp_f32_e32 v99, v99
	v_mfma_f32_32x32x16_bf16 v[16:31], v[152:155], v[178:181], v[16:31]
	v_exp_f32_e32 v100, v100
	v_exp_f32_e32 v101, v101
	v_exp_f32_e32 v102, v102
	v_exp_f32_e32 v103, v103
	v_mfma_f32_32x32x16_bf16 v[32:47], v[124:127], v[174:177], v[32:47]
	v_exp_f32_e32 v104, v104
	v_exp_f32_e32 v105, v105
	v_exp_f32_e32 v106, v106
	v_exp_f32_e32 v107, v107
	v_mfma_f32_32x32x16_bf16 v[48:63], v[124:127], v[178:181], v[48:63]
	v_exp_f32_e32 v108, v108
	v_exp_f32_e32 v109, v109
	v_exp_f32_e32 v110, v110
	v_exp_f32_e32 v111, v111
	v_mfma_f32_32x32x16_bf16 v[0:15], v[120:123], v[116:119], v[0:15]
	v_exp_f32_e32 v80, v80
	v_exp_f32_e32 v81, v81
	v_exp_f32_e32 v82, v82
	v_exp_f32_e32 v83, v83
	v_mfma_f32_32x32x16_bf16 v[16:31], v[120:123], v[112:115], v[16:31]
	v_exp_f32_e32 v84, v84
	v_exp_f32_e32 v85, v85
	v_exp_f32_e32 v86, v86
	v_exp_f32_e32 v87, v87
	v_mfma_f32_32x32x16_bf16 v[32:47], v[68:71], v[116:119], v[32:47]
	v_exp_f32_e32 v88, v88
	v_exp_f32_e32 v89, v89
	v_exp_f32_e32 v90, v90
	v_exp_f32_e32 v91, v91
	v_mfma_f32_32x32x16_bf16 v[48:63], v[68:71], v[112:115], v[48:63]
	v_exp_f32_e32 v92, v92
	v_exp_f32_e32 v93, v93
	v_exp_f32_e32 v94, v94
	v_exp_f32_e32 v95, v95
	v_add_u32_e32 v178, 0x10000, v173
	v_add_u32_e32 v179, 0xc000, v172
	v_add_f32_e32 v180, v96, v97
	v_add_f32_e32 v181, v98, v99
	v_add_f32_e32 v184, v100, v101
	v_add_f32_e32 v185, v102, v103
	s_waitcnt lgkmcnt(0)
; #define LAS __attribute__((address_space(3)))
; template <bool HAVE_PREV, bool HAVE_NEXT> __device__ __forceinline__ void dstep(f32x16& ca, f32x16& cb, f32x16& pa, f32x16& pb, const bf16x8 (&kf)[4], bf16x8 (&kn)[4], const LAS unsigned char* kbn, unsigned vpa, ...
;     const f32x16 z = {0.f, 0.f, 0.f, 0.f, 0.f, 0.f, 0.f, 0.f, 0.f, 0.f, 0.f, 0.f, 0.f, 0.f, 0.f, 0.f};
;     s16x4 vl[2][2], vh[2][2]; u32x4 wa[2], wb[2];
;     ca = __builtin_amdgcn_mfma_f32_32x32x16_bf16(kf[0], qr[0], z, 0, 0, 0);
;     float a0, a1, a2, a3, a4, a5, a6, a7, b0, b1, b2, b3, b4, b5, b6, b7;
;     if (HAVE_PREV) { a0 = fadd_s(pa[0], pa[1]); a1 = fadd_s(pa[2], pa[3]); a2 = fadd_s(pa[4], pa[5]); a3 = fadd_s(pa[6], pa[7]); a4 = fadd_s(pa[8], pa[9]); a5 = fadd_s(pa[10], pa[11]); a6 = fadd_s(pa[12], pa[13]); a7 = fadd_s(pa[14], pa[15]);
;         wa[0].x = cvtpk(pa[0], pa[1]); wa[0].y = cvtpk(pa[2], pa[3]); wa[0].z = cvtpk(pa[4], pa[5]); wa[0].w = cvtpk(pa[6], pa[7]); }
;     ATT_SB();
;     ca = __builtin_amdgcn_mfma_f32_32x32x16_bf16(kf[1], qr[1], ca, 0, 0, 0);
;     if (HAVE_PREV) {
;         ATT_TR(vl[0][0], vpa, 0); ATT_TR(vh[0][0], vpa, 512); ATT_TR(vl[1][0], vpa, 4096); ATT_TR(vh[1][0], vpa, 4096 + 512);
;         ATT_TR(vl[0][1], vpa, 1024); ATT_TR(vh[0][1], vpa, 1024 + 512); ATT_TR(vl[1][1], vpa, 4096 + 1024); ATT_TR(vh[1][1], vpa, 4096 + 1024 + 512);
;         a0 = fadd_s(a0, a1); a2 = fadd_s(a2, a3); a4 = fadd_s(a4, a5); a6 = fadd_s(a6, a7);
;         wa[1].x = cvtpk(pa[8], pa[9]); wa[1].y = cvtpk(pa[10], pa[11]); wa[1].z = cvtpk(pa[12], pa[13]); wa[1].w = cvtpk(pa[14], pa[15]);
;         a0 = fadd_s(a0, a2); a4 = fadd_s(a4, a6); }
;     ATT_SB();
;     cb = __builtin_amdgcn_mfma_f32_32x32x16_bf16(kf[2], qr[2], z, 0, 0, 0);
;     if (HAVE_PREV) { b0 = fadd_s(pb[0], pb[1]); b1 = fadd_s(pb[2], pb[3]); b2 = fadd_s(pb[4], pb[5]); b3 = fadd_s(pb[6], pb[7]); b4 = fadd_s(pb[8], pb[9]); b5 = fadd_s(pb[10], pb[11]); b6 = fadd_s(pb[12], pb[13]); b7 = fadd_s(pb[14], pb[15]);
; __device__ __forceinline__ void unit_diff(const P& p, LAS unsigned char* lds, const Src& S, float lam, bf16_t* orow, const int wid,
;                                           bf16x8 (&qr)[4], const bool pre  , const bool pn  , const Src& Sn) {
;     ...
;     ATT_WAITV(0); ATT_BAR();
;     dstep<true, false>(A0, B0, A1, B1, kA, kB, lds, lbase + sl_prev + voff + 2048, qr, o1, o2, l1, l2);
	v_mfma_f32_32x32x16_bf16 v[112:127], v[72:75], v[128:131], 0
	v_add_f32_e32 v186, v104, v105
	v_add_f32_e32 v187, v106, v107
	v_add_f32_e32 v188, v108, v109
	v_add_f32_e32 v189, v110, v111
	v_cvt_pk_bf16_f32 v148, v96, v97
	v_cvt_pk_bf16_f32 v149, v98, v99
	v_cvt_pk_bf16_f32 v150, v100, v101
	v_cvt_pk_bf16_f32 v151, v102, v103
	ds_read_b64_tr_b16 v[152:153], v179 offset:0
	ds_read_b64_tr_b16 v[154:155], v179 offset:512
	ds_read_b64_tr_b16 v[174:175], v179 offset:4096
	ds_read_b64_tr_b16 v[176:177], v179 offset:4608
	ds_read_b64_tr_b16 v[72:73], v179 offset:1024
	ds_read_b64_tr_b16 v[74:75], v179 offset:1536
	ds_read_b64_tr_b16 v[68:69], v179 offset:5120
	ds_read_b64_tr_b16 v[70:71], v179 offset:5632
	v_mfma_f32_32x32x16_bf16 v[112:127], v[76:79], v[132:135], v[112:127]
	v_add_f32_e32 v96, v180, v181
	v_add_f32_e32 v97, v184, v185
	v_add_f32_e32 v98, v186, v187
	v_add_f32_e32 v99, v188, v189
	v_cvt_pk_bf16_f32 v76, v104, v105
	v_cvt_pk_bf16_f32 v77, v106, v107
	v_cvt_pk_bf16_f32 v78, v108, v109
	v_cvt_pk_bf16_f32 v79, v110, v111
	s_nop 0
	v_add_f32_e32 v179, v96, v97
	v_add_f32_e32 v180, v98, v99
	v_mfma_f32_32x32x16_bf16 v[96:111], v[144:147], v[136:139], 0
	v_add_f32_e32 v144, v80, v81
	v_add_f32_e32 v145, v82, v83
	v_add_f32_e32 v146, v84, v85
	v_add_f32_e32 v147, v86, v87
	v_add_f32_e32 v181, v88, v89
	v_add_f32_e32 v184, v90, v91
	v_add_f32_e32 v185, v92, v93
	v_add_f32_e32 v186, v94, v95
	v_cvt_pk_bf16_f32 v80, v80, v81
	v_cvt_pk_bf16_f32 v81, v82, v83
	v_cvt_pk_bf16_f32 v82, v84, v85
	v_cvt_pk_bf16_f32 v83, v86, v87
	v_add_f32_e32 v84, v179, v180
	v_mfma_f32_32x32x16_bf16 v[96:111], v[64:67], v[140:143], v[96:111]
	v_add_f32_e32 v85, v144, v145
	v_add_f32_e32 v86, v146, v147
	v_add_f32_e32 v87, v181, v184
	v_add_f32_e32 v144, v185, v186
	v_cvt_pk_bf16_f32 v64, v88, v89
	v_cvt_pk_bf16_f32 v65, v90, v91
	v_cvt_pk_bf16_f32 v66, v92, v93
	v_cvt_pk_bf16_f32 v67, v94, v95
	s_nop 0
	v_add_f32_e32 v85, v85, v86
	v_add_f32_e32 v86, v87, v144
	v_add_f32_e32 v179, v182, v84
	s_nop 0
	v_add_f32_e32 v84, v85, v86
	s_waitcnt lgkmcnt(0)
	v_mfma_f32_32x32x16_bf16 v[0:15], v[148:151], v[152:155], v[0:15]
	v_add_u32_e32 v88, 0x10800, v173
	v_add_u32_e32 v92, 0x11000, v173
	v_add_u32_e32 v144, 0x11800, v173
	v_add_f32_e32 v180, v183, v84
	ds_read_b128 v[84:87], v178
	ds_read_b128 v[88:91], v88
	ds_read_b128 v[92:95], v92
	ds_read_b128 v[144:147], v144
	v_exp_f32_e32 v112, v112
	v_exp_f32_e32 v113, v113
	v_exp_f32_e32 v114, v114
	v_exp_f32_e32 v115, v115
	v_mfma_f32_32x32x16_bf16 v[16:31], v[148:151], v[174:177], v[16:31]
	v_exp_f32_e32 v116, v116
	v_exp_f32_e32 v117, v117
	v_exp_f32_e32 v118, v118
	v_exp_f32_e32 v119, v119
	v_mfma_f32_32x32x16_bf16 v[32:47], v[80:83], v[152:155], v[32:47]
	v_exp_f32_e32 v120, v120
	v_exp_f32_e32 v121, v121
	v_exp_f32_e32 v122, v122
	v_exp_f32_e32 v123, v123
	v_mfma_f32_32x32x16_bf16 v[48:63], v[80:83], v[174:177], v[48:63]
	v_exp_f32_e32 v124, v124
	v_exp_f32_e32 v125, v125
	v_exp_f32_e32 v126, v126
	v_exp_f32_e32 v127, v127
	v_mfma_f32_32x32x16_bf16 v[0:15], v[76:79], v[72:75], v[0:15]
	v_exp_f32_e32 v96, v96
	v_exp_f32_e32 v97, v97
	v_exp_f32_e32 v98, v98
	v_exp_f32_e32 v99, v99
	v_mfma_f32_32x32x16_bf16 v[16:31], v[76:79], v[68:71], v[16:31]
	v_exp_f32_e32 v100, v100
	v_exp_f32_e32 v101, v101
	v_exp_f32_e32 v102, v102
	v_exp_f32_e32 v103, v103
	v_mfma_f32_32x32x16_bf16 v[32:47], v[64:67], v[72:75], v[32:47]
	v_exp_f32_e32 v104, v104
	v_exp_f32_e32 v105, v105
	v_exp_f32_e32 v106, v106
	v_exp_f32_e32 v107, v107
	v_mfma_f32_32x32x16_bf16 v[48:63], v[64:67], v[68:71], v[48:63]
	v_exp_f32_e32 v108, v108
	v_exp_f32_e32 v109, v109
	v_exp_f32_e32 v110, v110
	v_exp_f32_e32 v111, v111
	s_waitcnt lgkmcnt(0)
	v_mfma_f32_32x32x16_bf16 v[64:79], v[84:87], v[128:131], 0
	s_waitcnt vmcnt(0)
	s_waitcnt lgkmcnt(0)
	s_barrier
; __device__ __forceinline__ unsigned cvtpk(float lo, float hi) { unsigned r; asm volatile("v_cvt_pk_bf16_f32 %0, %1, %2" : "=v"(r) : "v"(lo), "v"(hi)); return r; }
; #define ATT_BAR() do { asm volatile("s_waitcnt lgkmcnt(0)" ::: "memory"); __builtin_amdgcn_s_barrier(); asm volatile("" ::: "memory"); } while (0)
; #define ATT_TR(dst, addr, OFF) asm volatile("ds_read_b64_tr_b16 %0, %1 offset:%c2" : "=&v"(dst) : "v"(addr), "i"(OFF) : "memory")
; #define ATT_LGKM0() do { asm volatile("s_waitcnt lgkmcnt(0)" ::: "memory"); __builtin_amdgcn_sched_barrier(0); } while (0)
; __device__ __forceinline__ void unit_diff(const P& p, LAS unsigned char* lds, const Src& S, float lam, bf16_t* orow, const int wid,
;                                           bf16x8 (&qr)[4], const bool pre  , const bool pn  , const Src& Sn) {
;     ...
; #pragma unroll
;     for (int r = 8; r < 16; ++r) { A0[r] = 0.f; B0[r] = 0.f; }
;     {
;         l1 += ((A0[0] + A0[1]) + (A0[2] + A0[3])) + ((A0[4] + A0[5]) + (A0[6] + A0[7])); l2 += ((B0[0] + B0[1]) + (B0[2] + B0[3])) + ((B0[4] + B0[5]) + (B0[6] + B0[7]));
;         u32x4 wa, wb; wa.x = cvtpk(A0[0], A0[1]); wa.y = cvtpk(A0[2], A0[3]); wa.z = cvtpk(A0[4], A0[5]); wa.w = cvtpk(A0[6], A0[7]); wb.x = cvtpk(B0[0], B0[1]); wb.y = cvtpk(B0[2], B0[3]); wb.z = cvtpk(B0[4], B0[5]); wb.w = cvtpk(B0[6], B0[7]);
;         const unsigned vpa = lbase + sl_cur + voff;
; #pragma unroll
;         for (int d0 = 0; d0 < 2; ++d0) { s16x4 ml, mh; ATT_TR(ml, vpa, d0 * 4096); ATT_TR(mh, vpa, d0 * 4096 + 512); ATT_LGKM0(); const bf16x8 vf = ATT_VF(ml, mh);
;             o1[d0] = __builtin_amdgcn_mfma_f32_32x32x16_bf16(__builtin_bit_cast(bf16x8, wa), vf, o1[d0], 0, 0, 0); o2[d0] = __builtin_amdgcn_mfma_f32_32x32x16_bf16(__builtin_bit_cast(bf16x8, wb), vf, o2[d0], 0, 0, 0); } }
;     ATT_BAR();
;     bf16x8 qn[4];
;     if (pn) {
; #pragma unroll
;         for (int d0 = 0; d0 < 4; ++d0) qn[d0] = *(const bf16x8*)(Sn.q + (size_t)r32 * 64 + d0 * 16 + hi * 8);
;         ATT_DMA_S(Sn, 0, 0); ATT_DMA_S(Sn, 1, SLOTB); }
	v_add_u32_e32 v80, 0xc800, v172
	v_add_f32_e32 v81, v112, v113
	v_add_f32_e32 v82, v114, v115
	v_add_f32_e32 v83, v116, v117
	v_add_f32_e32 v84, v118, v119
	v_add_f32_e32 v85, v120, v121
	v_add_f32_e32 v86, v122, v123
	v_add_f32_e32 v87, v124, v125
	v_add_f32_e32 v173, v126, v127
	v_cvt_pk_bf16_f32 v148, v112, v113
	v_cvt_pk_bf16_f32 v149, v114, v115
	v_cvt_pk_bf16_f32 v150, v116, v117
	v_cvt_pk_bf16_f32 v151, v118, v119
	ds_read_b64_tr_b16 v[152:153], v80 offset:0
	ds_read_b64_tr_b16 v[154:155], v80 offset:512
	ds_read_b64_tr_b16 v[174:175], v80 offset:4096
	v_mfma_f32_32x32x16_bf16 v[64:79], v[88:91], v[132:135], v[64:79]
	ds_read_b64_tr_b16 v[176:177], v80 offset:4608
	ds_read_b64_tr_b16 v[116:117], v80 offset:1024
	ds_read_b64_tr_b16 v[118:119], v80 offset:1536
	ds_read_b64_tr_b16 v[112:113], v80 offset:5120
	ds_read_b64_tr_b16 v[114:115], v80 offset:5632
	v_add_f32_e32 v80, v81, v82
	v_add_f32_e32 v81, v83, v84
	v_add_f32_e32 v82, v85, v86
	v_add_f32_e32 v83, v87, v173
	v_cvt_pk_bf16_f32 v120, v120, v121
	v_cvt_pk_bf16_f32 v121, v122, v123
	v_cvt_pk_bf16_f32 v122, v124, v125
	v_cvt_pk_bf16_f32 v123, v126, v127
	s_nop 0
	v_add_f32_e32 v173, v80, v81
	v_add_f32_e32 v178, v82, v83
	v_mfma_f32_32x32x16_bf16 v[80:95], v[92:95], v[136:139], 0
	v_add_f32_e32 v181, v96, v97
	v_add_f32_e32 v182, v98, v99
	v_add_f32_e32 v183, v100, v101
	v_add_f32_e32 v184, v102, v103
	v_add_f32_e32 v185, v104, v105
	v_add_f32_e32 v186, v106, v107
	v_add_f32_e32 v187, v108, v109
	v_add_f32_e32 v188, v110, v111
	v_cvt_pk_bf16_f32 v124, v96, v97
	v_cvt_pk_bf16_f32 v125, v98, v99
	v_cvt_pk_bf16_f32 v126, v100, v101
	v_cvt_pk_bf16_f32 v127, v102, v103
	v_add_f32_e32 v96, v173, v178
	v_mfma_f32_32x32x16_bf16 v[80:95], v[144:147], v[140:143], v[80:95]
	v_add_f32_e32 v97, v181, v182
	v_add_f32_e32 v102, v183, v184
	v_add_f32_e32 v103, v185, v186
	v_add_f32_e32 v144, v187, v188
	v_cvt_pk_bf16_f32 v98, v104, v105
	v_cvt_pk_bf16_f32 v99, v106, v107
	v_cvt_pk_bf16_f32 v100, v108, v109
	v_cvt_pk_bf16_f32 v101, v110, v111
	s_nop 0
	v_add_f32_e32 v97, v97, v102
	v_add_f32_e32 v102, v103, v144
	v_add_f32_e32 v96, v179, v96
	s_nop 0
	v_add_f32_e32 v97, v97, v102
	s_waitcnt lgkmcnt(0)
	v_mfma_f32_32x32x16_bf16 v[0:15], v[148:151], v[152:155], v[0:15]
	s_nop 5
	v_exp_f32_e32 v64, v64
	v_exp_f32_e32 v65, v65
	v_exp_f32_e32 v66, v66
	v_exp_f32_e32 v67, v67
	v_add_f32_e32 v97, v180, v97
	v_mfma_f32_32x32x16_bf16 v[16:31], v[148:151], v[174:177], v[16:31]
	v_exp_f32_e32 v68, v68
	v_exp_f32_e32 v69, v69
	v_exp_f32_e32 v70, v70
	v_exp_f32_e32 v71, v71
	v_mfma_f32_32x32x16_bf16 v[32:47], v[124:127], v[152:155], v[32:47]
	v_exp_f32_e32 v72, v72
	v_exp_f32_e32 v73, v73
	v_exp_f32_e32 v74, v74
	v_exp_f32_e32 v75, v75
	v_mfma_f32_32x32x16_bf16 v[48:63], v[124:127], v[174:177], v[48:63]
	v_exp_f32_e32 v76, v76
	v_exp_f32_e32 v77, v77
	v_exp_f32_e32 v78, v78
	v_exp_f32_e32 v79, v79
	v_mfma_f32_32x32x16_bf16 v[0:15], v[120:123], v[116:119], v[0:15]
	v_exp_f32_e32 v80, v80
	v_exp_f32_e32 v81, v81
	v_exp_f32_e32 v82, v82
	v_exp_f32_e32 v83, v83
	v_mfma_f32_32x32x16_bf16 v[16:31], v[120:123], v[112:115], v[16:31]
	v_exp_f32_e32 v84, v84
	v_exp_f32_e32 v85, v85
	v_exp_f32_e32 v86, v86
	v_exp_f32_e32 v87, v87
	v_mfma_f32_32x32x16_bf16 v[32:47], v[98:101], v[116:119], v[32:47]
	v_exp_f32_e32 v88, v88
	v_exp_f32_e32 v89, v89
	v_exp_f32_e32 v90, v90
	v_exp_f32_e32 v91, v91
	v_mfma_f32_32x32x16_bf16 v[48:63], v[98:101], v[112:115], v[48:63]
	v_exp_f32_e32 v92, v92
	v_exp_f32_e32 v93, v93
	v_exp_f32_e32 v94, v94
	v_exp_f32_e32 v95, v95
	v_cvt_pk_bf16_f32 v72, v64, v65
	v_cvt_pk_bf16_f32 v73, v66, v67
	v_cvt_pk_bf16_f32 v74, v68, v69
	v_cvt_pk_bf16_f32 v75, v70, v71
	s_nop 0
	v_cvt_pk_bf16_f32 v76, v80, v81
	v_cvt_pk_bf16_f32 v77, v82, v83
	v_cvt_pk_bf16_f32 v78, v84, v85
	v_cvt_pk_bf16_f32 v79, v86, v87
	v_add_u32_e32 v92, 0x10000, v172
	ds_read_b64_tr_b16 v[88:89], v92 offset:0
	ds_read_b64_tr_b16 v[90:91], v92 offset:512
	s_waitcnt lgkmcnt(0)
	s_nop 0
	v_mfma_f32_32x32x16_bf16 v[0:15], v[72:75], v[88:91], v[0:15]
	v_mfma_f32_32x32x16_bf16 v[32:47], v[76:79], v[88:91], v[32:47]
	ds_read_b64_tr_b16 v[88:89], v92 offset:4096
	ds_read_b64_tr_b16 v[90:91], v92 offset:4608
	s_waitcnt lgkmcnt(0)
	s_nop 0
	v_mfma_f32_32x32x16_bf16 v[16:31], v[72:75], v[88:91], v[16:31]
	s_waitcnt lgkmcnt(0)
	s_barrier
	s_and_b64 vcc, exec, s[56:57]
	v_mfma_f32_32x32x16_bf16 v[48:63], v[76:79], v[88:91], v[48:63]
	s_cbranch_vccz .LBB7_441
	s_cselect_b32 s11, s60, s95
	s_ashr_i32 s10, s11, 4
	s_lshl_b32 s11, s11, 8
	s_and_b32 s11, s11, 0xf00
	s_add_i32 s36, s11, s90
	s_ashr_i32 s11, s10, 31
	s_lshl_b64 s[10:11], s[10:11], 19
	s_mov_b32 s37, s9
	s_add_u32 s13, s34, s10
	s_addc_u32 s53, s35, s11
	s_lshl_b64 s[36:37], s[36:37], 7
	s_add_u32 s36, s13, s36
	s_addc_u32 s37, s53, s37
	s_add_u32 s58, s6, s10
	s_addc_u32 s59, s7, s11
	s_add_u32 s10, s92, s10
	v_lshl_add_u64 v[72:73], s[36:37], 0, v[156:157]
	s_mov_b32 m0, s91
	s_addc_u32 s11, s4, s11
	v_lshl_add_u64 v[72:73], v[158:159], 1, v[72:73]
	v_lshl_add_u64 v[98:99], s[58:59], 0, v[160:161]
	global_load_dwordx4 v[92:95], v[72:73], off
	global_load_dwordx4 v[88:91], v[72:73], off offset:32
	global_load_dwordx4 v[76:79], v[72:73], off offset:64
	s_nop 0
	global_load_dwordx4 v[72:75], v[72:73], off offset:96
	v_lshl_add_u64 v[100:101], s[10:11], 0, v[160:161]
	global_load_lds_dwordx4 v[98:99], off
	s_mov_b32 m0, s15
	v_lshl_add_u64 v[98:99], v[98:99], 0, s[46:47]
	global_load_lds_dwordx4 v[100:101], off
	s_add_i32 m0, s91, 0x4000
	s_nop 0
	global_load_lds_dwordx4 v[98:99], off
	v_lshl_add_u64 v[98:99], v[100:101], 0, s[46:47]
	s_add_i32 m0, s91, 0x6000
	s_nop 0
	global_load_lds_dwordx4 v[98:99], off
